# baseline (speedup 1.0000x reference)
_Z15gemm_qkv_kernelPKDF16_S0_PDF16_S1_S1_PKfS3_S3_S3_S3_S1_PKiPyPj:
	s_load_dwordx8 s[36:43], s[0:1], 0x40
	s_load_dwordx4 s[28:31], s[0:1], 0x60
	s_mov_b64 s[4:5], -1
	s_cmpk_lt_i32 s2, 0x40
	s_movk_i32 s3, 0xc0
	s_cbranch_scc1 .LBB1_30
	s_add_i32 s2, s2, 0xffffffc0
	v_lshlrev_b32_e32 v1, 4, v0
	v_and_b32_e32 v2, 32, v0
	v_lshrrev_b32_e32 v4, 1, v0
	v_lshrrev_b32_e32 v5, 5, v0
	v_or_b32_e32 v13, 0x2000, v1
	s_load_dwordx16 s[12:27], s[0:1], 0x0
	v_bfe_u32 v12, v0, 2, 4
	v_bitop3_b32 v10, v1, v2, 48 bitop3:0x6c
	v_and_b32_e32 v4, 24, v4
	v_and_b32_e32 v5, 4, v5
	v_bfe_u32 v6, v0, 2, 2
	v_lshrrev_b32_e32 v1, 7, v13
	s_movk_i32 s0, 0x70
	s_ashr_i32 s33, s2, 31
	v_lshrrev_b32_e32 v3, 2, v0
	v_and_b32_e32 v11, 64, v0
	v_or3_b32 v4, v5, v6, v4
	v_and_or_b32 v1, v1, s0, v12
	s_lshr_b32 s0, s33, 29
	v_readfirstlane_b32 s1, v0
	v_or_b32_e32 v2, v10, v11
	v_and_or_b32 v3, v3, 64, v4
	s_add_i32 s0, s2, s0
	s_lshr_b32 s10, s1, 6
	v_lshl_or_b32 v164, v3, 12, v2
	v_lshrrev_b32_e32 v3, 6, v13
	s_ashr_i32 s4, s0, 3
	s_and_b32 s0, s0, -8
	v_and_or_b32 v3, v3, s3, v4
	s_lshr_b32 s44, s1, 8
	s_lshl_b32 s3, s10, 10
	s_sub_i32 s0, s2, s0
	s_cmp_lt_i32 s0, 0
	s_cselect_b32 s5, 25, 24
	s_mul_i32 s0, s0, s5
	s_add_i32 s0, s0, s4
	s_mul_hi_i32 s4, s0, 0x2aaaaaab
	s_lshr_b32 s5, s4, 31
	s_ashr_i32 s4, s4, 4
	s_add_i32 s4, s4, s5
	s_lshl_b32 s5, s4, 3
	s_mulk_i32 s4, 0x60
	s_sub_i32 s4, s0, s4
	s_bfe_i32 s0, s4, 0x80000
	s_bfe_u32 s0, s0, 0x3000c
	s_add_i32 s6, s4, s0
	s_bfe_i32 s0, s6, 0x80000
	s_and_b32 s6, s6, 0xf8
	s_sub_i32 s4, s4, s6
	s_sext_i32_i16 s0, s0
	s_sext_i32_i8 s4, s4
	s_lshr_b32 s0, s0, 3
	s_add_i32 s4, s5, s4
	s_ashr_i32 s5, s4, 31
	s_bfe_i64 s[8:9], s[0:1], 0x100000
	s_lshl_b64 s[6:7], s[4:5], 20
	s_lshl_b64 s[8:9], s[8:9], 20
	s_waitcnt lgkmcnt(0)
	s_mov_b32 s84, 0
	s_add_u32 s80, s20, 0x408000
	s_addc_u32 s81, s21, 0
	v_and_b32_e32 v241, 63, v0
	v_lshlrev_b32_e32 v241, 2, v241
	s_add_u32 s8, s14, s8
	s_addc_u32 s9, s15, s9
	s_add_i32 s58, s3, 0
	s_add_i32 m0, s58, 0x10000
	v_lshl_or_b32 v168, v3, 12, v2
	global_load_lds_dwordx4 v164, s[8:9]
	s_add_i32 m0, s58, 0x12000
	s_add_u32 s34, s8, 0x20000
	global_load_lds_dwordx4 v168, s[8:9]
	s_addc_u32 s35, s9, 0
	s_add_i32 m0, s58, 0x14000
	v_lshrrev_b32_e32 v5, 3, v0
	global_load_lds_dwordx4 v164, s[34:35]
	s_add_i32 m0, s58, 0x16000
	s_add_u32 s6, s12, s6
	v_and_or_b32 v5, v5, 48, v12
	s_addc_u32 s7, s13, s7
	s_add_i32 s59, s58, 0x2000
	v_lshl_or_b32 v162, v5, 12, v2
	global_load_lds_dwordx4 v168, s[34:35]
	s_mov_b32 m0, s58
	s_add_u32 s34, s6, 0x80000
	v_lshl_or_b32 v166, v1, 12, v2
	global_load_lds_dwordx4 v162, s[6:7]
	s_mov_b32 m0, s59
	s_addc_u32 s35, s7, 0
	s_add_i32 s60, s58, 0x4000
	global_load_lds_dwordx4 v166, s[6:7]
	s_mov_b32 m0, s60
	s_add_i32 s61, s58, 0x6000
	global_load_lds_dwordx4 v162, s[34:35]
	s_mov_b32 m0, s61
	v_mov_b32_e32 v171, 0
	global_load_lds_dwordx4 v166, s[34:35]
	v_mov_b32_e32 v165, v171
	v_mov_b32_e32 v169, v171
	v_mov_b32_e32 v163, v171
	v_mov_b32_e32 v167, v171
	s_cmp_eq_u32 s44, 1
	s_mov_b32 s11, 0
	v_lshl_add_u64 v[8:9], s[8:9], 0, v[164:165]
	v_lshl_add_u64 v[6:7], s[8:9], 0, v[168:169]
	v_lshl_add_u64 v[2:3], s[6:7], 0, v[162:163]
	s_cselect_b64 s[34:35], -1, 0
	s_cmp_lg_u32 s44, 1
	v_lshl_add_u64 v[4:5], s[6:7], 0, v[166:167]
	s_cbranch_scc1 .LBB1_3
	s_barrier

.LBB1_25:
	s_waitcnt lgkmcnt(0)
	v_add_f32_e32 v170, v170, v205
	v_fmamk_f32 v170, v170, 0x3c800000, v195
	v_mul_f32_e32 v185, 0x4f800000, v170
	v_cmp_gt_f32_e32 vcc, s70, v170
	s_lshl_b32 s10, s8, 1
	s_nop 0
	v_cndmask_b32_e32 v170, v170, v185, vcc
	v_sqrt_f32_e32 v185, v170
	s_nop 0
	v_add_u32_e32 v204, -1, v185
	v_fma_f32 v206, -v204, v185, v170
	v_add_u32_e32 v205, 1, v185
	v_cmp_ge_f32_e64 s[4:5], 0, v206
	s_nop 1
	v_cndmask_b32_e64 v204, v185, v204, s[4:5]
	v_fma_f32 v185, -v205, v185, v170
	v_cmp_lt_f32_e64 s[4:5], 0, v185
	s_nop 1
	v_cndmask_b32_e64 v185, v204, v205, s[4:5]
	v_mul_f32_e32 v204, 0x37800000, v185
	v_cndmask_b32_e32 v185, v185, v204, vcc
	v_cmp_class_f32_e32 vcc, v170, v196
	s_nop 1
	v_cndmask_b32_e32 v170, v185, v170, vcc
	v_div_scale_f32 v185, s[4:5], v170, v170, v200
	v_rcp_f32_e32 v204, v185
	s_nop 0
	v_fma_f32 v205, -v185, v204, 1.0
	v_fmac_f32_e32 v204, v205, v204
	v_div_scale_f32 v205, vcc, v200, v170, v200
	v_mul_f32_e32 v206, v205, v204
	v_fma_f32 v207, -v185, v206, v205
	v_fmac_f32_e32 v206, v207, v204
	v_fma_f32 v185, -v185, v206, v205
	v_div_fmas_f32 v185, v185, v204, v206
	v_div_fixup_f32 v170, v185, v170, v200
	v_pk_mul_f32 v[212:213], v[14:15], v[170:171] op_sel_hi:[1,0]
	v_pk_mul_f32 v[214:215], v[16:17], v[170:171] op_sel_hi:[1,0]
	v_pk_mul_f32 v[216:217], v[10:11], v[170:171] op_sel_hi:[1,0]
	v_pk_mul_f32 v[218:219], v[12:13], v[170:171] op_sel_hi:[1,0]
	v_pk_mul_f32 v[204:205], v[40:41], v[170:171] op_sel_hi:[1,0]
	v_pk_mul_f32 v[206:207], v[38:39], v[170:171] op_sel_hi:[1,0]
	v_pk_mul_f32 v[208:209], v[36:37], v[170:171] op_sel_hi:[1,0]
	v_pk_mul_f32 v[210:211], v[34:35], v[170:171] op_sel_hi:[1,0]
	v_pk_mul_f32 v[214:215], v[136:137], v[214:215]
	v_pk_mul_f32 v[212:213], v[134:135], v[212:213]
	v_pk_mul_f32 v[218:219], v[132:133], v[218:219]
	v_pk_mul_f32 v[216:217], v[130:131], v[216:217]
	v_pk_mul_f32 v[206:207], v[142:143], v[206:207]
	v_pk_mul_f32 v[204:205], v[144:145], v[204:205]
	v_pk_mul_f32 v[210:211], v[138:139], v[210:211]
	v_pk_mul_f32 v[208:209], v[140:141], v[208:209]
	s_waitcnt vmcnt(0)
	v_pk_mul_f32 v[220:221], v[158:159], v[212:213]
	v_pk_mul_f32 v[222:223], v[160:161], v[214:215]
	v_pk_mul_f32 v[224:225], v[150:151], v[216:217]
	v_pk_mul_f32 v[226:227], v[152:153], v[218:219]
	v_pk_fma_f32 v[222:223], v[156:157], v[204:205], v[222:223] neg_lo:[0,0,1] neg_hi:[0,0,1]
	v_pk_fma_f32 v[220:221], v[154:155], v[206:207], v[220:221] neg_lo:[0,0,1] neg_hi:[0,0,1]
	v_pk_fma_f32 v[226:227], v[148:149], v[208:209], v[226:227] neg_lo:[0,0,1] neg_hi:[0,0,1]
	v_pk_fma_f32 v[224:225], v[146:147], v[210:211], v[224:225] neg_lo:[0,0,1] neg_hi:[0,0,1]
	v_pk_mul_f32 v[154:155], v[154:155], v[212:213]
	v_pk_mul_f32 v[156:157], v[156:157], v[214:215]
	v_pk_mul_f32 v[146:147], v[146:147], v[216:217]
	v_pk_mul_f32 v[148:149], v[148:149], v[218:219]
	v_ashrrev_i32_e32 v185, 31, v184
	v_pk_fma_f32 v[156:157], v[160:161], v[204:205], v[156:157]
	v_pk_fma_f32 v[154:155], v[158:159], v[206:207], v[154:155]
	v_pk_fma_f32 v[158:159], v[152:153], v[208:209], v[148:149]
	v_pk_fma_f32 v[152:153], v[150:151], v[210:211], v[146:147]
	v_lshl_add_u64 v[160:161], v[184:185], 1, s[6:7]
	v_cvt_pk_f16_f32 v146, v220, v221
	v_cvt_pk_f16_f32 v147, v222, v223
	v_cvt_pk_f16_f32 v148, v224, v225
	v_cvt_pk_f16_f32 v149, v226, v227
	v_cvt_pk_f16_f32 v150, v154, v155
	v_cvt_pk_f16_f32 v151, v156, v157
	v_cvt_pk_f16_f32 v152, v152, v153
	v_cvt_pk_f16_f32 v153, v158, v159
	global_store_dwordx4 v[160:161], v[146:149], off sc1
	v_add_u32_e32 v208, 0xb0, v199
	v_and_b32_e32 v209, 0x7ff, v208
	v_lshl_add_u64 v[146:147], v[160:161], 0, s[10:11]
	global_store_dwordx4 v[146:147], v[150:153], off sc1
	v_mul_f32_e32 v146, v23, v23
	v_mul_f32_e32 v147, v25, v25
	v_fmac_f32_e32 v146, v22, v22
	v_fmac_f32_e32 v147, v24, v24
	v_add_f32_e32 v152, v146, v147
	v_pk_mul_f32 v[146:147], v[20:21], v[20:21]
	v_pk_mul_f32 v[148:149], v[18:19], v[18:19]
	v_mov_b32_e32 v150, v146
	v_mov_b32_e32 v151, v148
	v_mov_b32_e32 v148, v147
	v_pk_add_f32 v[146:147], v[150:151], v[148:149]
	v_lshlrev_b32_e32 v170, 7, v209
	v_add_f32_e32 v147, v152, v147
	v_lshl_add_u64 v[158:159], v[172:173], 0, v[170:171]
	v_lshl_add_u64 v[150:151], v[174:175], 0, v[170:171]
	v_add_f32_e32 v210, v146, v147
	global_load_dwordx4 v[146:149], v[150:151], off offset:16
	s_nop 0
	global_load_dwordx4 v[150:153], v[150:151], off
	s_nop 0
	global_load_dwordx4 v[154:157], v[158:159], off offset:16
	s_nop 0
	global_load_dwordx4 v[158:161], v[158:159], off
	v_pk_mul_f32 v[184:185], v[8:9], v[8:9]
	v_pk_mul_f32 v[204:205], v[6:7], v[6:7]
	v_mov_b32_e32 v206, v184
	v_mov_b32_e32 v207, v204
	v_mov_b32_e32 v204, v185
	v_pk_add_f32 v[184:185], v[206:207], v[204:205]
	v_pk_mul_f32 v[204:205], v[2:3], v[2:3]
	v_add_f32_e32 v170, v210, v185
	v_add_f32_e32 v170, v184, v170
	v_pk_mul_f32 v[184:185], v[4:5], v[4:5]
	v_mov_b32_e32 v207, v204
	v_mov_b32_e32 v206, v184
	v_mov_b32_e32 v204, v185
	v_pk_add_f32 v[184:185], v[206:207], v[204:205]
	s_nop 0
	v_add_f32_e32 v170, v185, v170
	v_add_f32_e32 v170, v184, v170
	ds_bpermute_b32 v184, v201, v170
	s_waitcnt lgkmcnt(0)
	v_add_f32_e32 v170, v170, v184
	ds_bpermute_b32 v184, v202, v170
	s_waitcnt lgkmcnt(0)
	v_add_f32_e32 v170, v170, v184
	v_fmamk_f32 v170, v170, 0x3c800000, v195
	v_mul_f32_e32 v184, 0x4f800000, v170
	v_cmp_gt_f32_e32 vcc, s70, v170
	s_nop 1
	v_cndmask_b32_e32 v170, v170, v184, vcc
	v_sqrt_f32_e32 v184, v170
	s_nop 0
	v_add_u32_e32 v185, -1, v184
	v_fma_f32 v201, -v185, v184, v170
	v_cmp_ge_f32_e64 s[4:5], 0, v201
	v_add_u32_e32 v201, 1, v184
	s_nop 0
	v_cndmask_b32_e64 v185, v184, v185, s[4:5]
	v_fma_f32 v184, -v201, v184, v170
	v_cmp_lt_f32_e64 s[4:5], 0, v184
	s_nop 1
	v_cndmask_b32_e64 v184, v185, v201, s[4:5]
	v_mul_f32_e32 v185, 0x37800000, v184
	v_cndmask_b32_e32 v184, v184, v185, vcc
	v_cmp_class_f32_e32 vcc, v170, v196
	s_nop 1
	v_cndmask_b32_e32 v170, v184, v170, vcc
	v_div_scale_f32 v184, s[4:5], v170, v170, v200
	v_rcp_f32_e32 v185, v184
	s_nop 0
	v_fma_f32 v201, -v184, v185, 1.0
	v_fmac_f32_e32 v185, v201, v185
	v_div_scale_f32 v201, vcc, v200, v170, v200
	v_mul_f32_e32 v202, v201, v185
	v_fma_f32 v204, -v184, v202, v201
	v_fmac_f32_e32 v202, v204, v185
	v_fma_f32 v184, -v184, v202, v201
	v_div_fmas_f32 v184, v184, v185, v202
	v_div_fixup_f32 v170, v184, v170, v200
	v_pk_mul_f32 v[184:185], v[24:25], v[170:171] op_sel_hi:[1,0]
	v_pk_mul_f32 v[200:201], v[22:23], v[170:171] op_sel_hi:[1,0]
	v_pk_mul_f32 v[144:145], v[144:145], v[184:185]
	v_pk_mul_f32 v[184:185], v[20:21], v[170:171] op_sel_hi:[1,0]
	v_pk_mul_f32 v[142:143], v[142:143], v[200:201]
	v_pk_mul_f32 v[140:141], v[140:141], v[184:185]
	v_pk_mul_f32 v[184:185], v[6:7], v[170:171] op_sel_hi:[1,0]
	v_pk_mul_f32 v[200:201], v[18:19], v[170:171] op_sel_hi:[1,0]
	v_pk_mul_f32 v[134:135], v[134:135], v[184:185]
	v_pk_mul_f32 v[184:185], v[2:3], v[170:171] op_sel_hi:[1,0]
	v_pk_mul_f32 v[138:139], v[138:139], v[200:201]
	v_pk_mul_f32 v[130:131], v[130:131], v[184:185]
	v_pk_mul_f32 v[200:201], v[8:9], v[170:171] op_sel_hi:[1,0]
	s_waitcnt vmcnt(3)
	v_pk_mul_f32 v[204:205], v[146:147], v[130:131]
	s_waitcnt vmcnt(1)
	v_pk_mul_f32 v[130:131], v[154:155], v[130:131]
	v_pk_mul_f32 v[136:137], v[136:137], v[200:201]
	v_pk_mul_f32 v[200:201], v[4:5], v[170:171] op_sel_hi:[1,0]
	v_pk_fma_f32 v[204:205], v[154:155], v[138:139], v[204:205] neg_lo:[0,0,1] neg_hi:[0,0,1]
	v_pk_fma_f32 v[138:139], v[146:147], v[138:139], v[130:131]
	v_lshlrev_b32_e32 v130, 6, v209
	v_lshlrev_b32_e32 v131, 3, v208
	v_pk_mul_f32 v[132:133], v[132:133], v[200:201]
	v_and_b32_e32 v130, s37, v130
	v_and_b32_e32 v131, s9, v131
	v_pk_mul_f32 v[184:185], v[150:151], v[134:135]
	v_pk_mul_f32 v[200:201], v[152:153], v[136:137]
	v_pk_mul_f32 v[206:207], v[148:149], v[132:133]
	v_or3_b32 v130, v131, v203, v130
	s_waitcnt vmcnt(0)
	v_pk_fma_f32 v[200:201], v[160:161], v[144:145], v[200:201] neg_lo:[0,0,1] neg_hi:[0,0,1]
	v_pk_fma_f32 v[184:185], v[158:159], v[142:143], v[184:185] neg_lo:[0,0,1] neg_hi:[0,0,1]
	v_pk_fma_f32 v[206:207], v[156:157], v[140:141], v[206:207] neg_lo:[0,0,1] neg_hi:[0,0,1]
	v_pk_mul_f32 v[134:135], v[158:159], v[134:135]
	v_pk_mul_f32 v[136:137], v[160:161], v[136:137]
	v_pk_mul_f32 v[132:133], v[156:157], v[132:133]
	v_ashrrev_i32_e32 v131, 31, v130
	v_pk_fma_f32 v[136:137], v[152:153], v[144:145], v[136:137]
	v_pk_fma_f32 v[134:135], v[150:151], v[142:143], v[134:135]
	v_pk_fma_f32 v[140:141], v[148:149], v[140:141], v[132:133]
	v_lshl_add_u64 v[142:143], v[130:131], 1, s[6:7]
	v_cvt_pk_f16_f32 v130, v184, v185
	v_cvt_pk_f16_f32 v131, v200, v201
	v_cvt_pk_f16_f32 v132, v204, v205
	v_cvt_pk_f16_f32 v133, v206, v207
	v_cvt_pk_f16_f32 v134, v134, v135
	v_cvt_pk_f16_f32 v135, v136, v137
	v_cvt_pk_f16_f32 v136, v138, v139
	v_cvt_pk_f16_f32 v137, v140, v141
	global_store_dwordx4 v[142:143], v[130:133], off sc1
	s_nop 1
	v_lshl_add_u64 v[130:131], v[142:143], 0, s[10:11]
	global_store_dwordx4 v[130:131], v[134:137], off sc1
	s_cmp_lg_u32 s84, 0
	s_cbranch_scc1 .LBB1_14
	s_mov_b32 s84, 1
	s_waitcnt vmcnt(0) lgkmcnt(0)
	s_branch .LBB1_15

	.amdhsa_kernel _Z15gemm_qkv_kernelPKDF16_S0_PDF16_S1_S1_PKfS3_S3_S3_S3_S1_PKiPyPj
		.amdhsa_group_segment_fixed_size 0
		.amdhsa_private_segment_fixed_size 0
		.amdhsa_kernarg_size 112
		.amdhsa_user_sgpr_count 2
		.amdhsa_user_sgpr_dispatch_ptr 0
		.amdhsa_user_sgpr_queue_ptr 0
		.amdhsa_user_sgpr_kernarg_segment_ptr 1
		.amdhsa_user_sgpr_dispatch_id 0
		.amdhsa_user_sgpr_kernarg_preload_length 0
		.amdhsa_user_sgpr_kernarg_preload_offset 0
		.amdhsa_user_sgpr_private_segment_size 0
		.amdhsa_uses_dynamic_stack 0
		.amdhsa_enable_private_segment 0
		.amdhsa_system_sgpr_workgroup_id_x 1
		.amdhsa_system_sgpr_workgroup_id_y 0
		.amdhsa_system_sgpr_workgroup_id_z 0
		.amdhsa_system_sgpr_workgroup_info 0
		.amdhsa_system_vgpr_workitem_id 0
		.amdhsa_next_free_vgpr 244
		.amdhsa_next_free_sgpr 85
		.amdhsa_accum_offset 244
		.amdhsa_reserve_vcc 1
		.amdhsa_float_round_mode_32 0
		.amdhsa_float_round_mode_16_64 0
		.amdhsa_float_denorm_mode_32 3
		.amdhsa_float_denorm_mode_16_64 3
		.amdhsa_dx10_clamp 1
		.amdhsa_ieee_mode 1
		.amdhsa_fp16_overflow 0
		.amdhsa_tg_split 0
		.amdhsa_exception_fp_ieee_invalid_op 0
		.amdhsa_exception_fp_denorm_src 0
		.amdhsa_exception_fp_ieee_div_zero 0
		.amdhsa_exception_fp_ieee_overflow 0
		.amdhsa_exception_fp_ieee_underflow 0
		.amdhsa_exception_fp_ieee_inexact 0
		.amdhsa_exception_int_div_zero 0
	.end_amdhsa_kernel

amdhsa.kernels:
  - .agpr_count:     0
    .args:
      - .actual_access:  read_only
        .address_space:  global
        .offset:         0
        .size:           8
        .value_kind:     global_buffer
      - .actual_access:  read_only
        .address_space:  global
        .offset:         8
        .size:           8
        .value_kind:     global_buffer
      - .actual_access:  read_only
        .address_space:  global
        .offset:         16
        .size:           8
        .value_kind:     global_buffer
      - .actual_access:  write_only
        .address_space:  global
        .offset:         24
        .size:           8
        .value_kind:     global_buffer
      - .actual_access:  write_only
        .address_space:  global
        .offset:         32
        .size:           8
        .value_kind:     global_buffer
      - .actual_access:  write_only
        .address_space:  global
        .offset:         40
        .size:           8
        .value_kind:     global_buffer
      - .actual_access:  write_only
        .address_space:  global
        .offset:         48
        .size:           8
        .value_kind:     global_buffer
    .group_segment_fixed_size: 0
    .kernarg_segment_align: 8
    .kernarg_segment_size: 56
    .language:       OpenCL C
    .language_version:
      - 2
      - 0
    .max_flat_workgroup_size: 1024
    .name:           _Z11prep_kernelPKfS0_PKiPDF16_S3_PfS4_
    .private_segment_fixed_size: 0
    .sgpr_count:     24
    .sgpr_spill_count: 0
    .symbol:         _Z11prep_kernelPKfS0_PKiPDF16_S3_PfS4_.kd
    .uniform_work_group_size: 1
    .uses_dynamic_stack: false
    .vgpr_count:     40
    .vgpr_spill_count: 0
    .wavefront_size: 64
  - .agpr_count:     0
    .args:
      - .address_space:  global
        .offset:         0
        .size:           8
        .value_kind:     global_buffer
      - .address_space:  global
        .offset:         8
        .size:           8
        .value_kind:     global_buffer
      - .address_space:  global
        .offset:         16
        .size:           8
        .value_kind:     global_buffer
      - .address_space:  global
        .offset:         24
        .size:           8
        .value_kind:     global_buffer
      - .address_space:  global
        .offset:         32
        .size:           8
        .value_kind:     global_buffer
      - .address_space:  global
        .offset:         40
        .size:           8
        .value_kind:     global_buffer
      - .address_space:  global
        .offset:         48
        .size:           8
        .value_kind:     global_buffer
      - .address_space:  global
        .offset:         56
        .size:           8
        .value_kind:     global_buffer
      - .address_space:  global
        .offset:         64
        .size:           8
        .value_kind:     global_buffer
      - .address_space:  global
        .offset:         72
        .size:           8
        .value_kind:     global_buffer
      - .address_space:  global
        .offset:         80
        .size:           8
        .value_kind:     global_buffer
      - .address_space:  global
        .offset:         88
        .size:           8
        .value_kind:     global_buffer
      - .address_space:  global
        .offset:         96
        .size:           8
        .value_kind:     global_buffer
      - .address_space:  global
        .offset:         104
        .size:           8
        .value_kind:     global_buffer
    .group_segment_fixed_size: 0
    .kernarg_segment_align: 8
    .kernarg_segment_size: 112
    .language:       OpenCL C
    .language_version:
      - 2
      - 0
    .max_flat_workgroup_size: 512
    .name:           _Z15gemm_qkv_kernelPKDF16_S0_PDF16_S1_S1_PKfS3_S3_S3_S3_S1_PKiPyPj
    .private_segment_fixed_size: 0
    .sgpr_count:     91
    .sgpr_spill_count: 0
    .symbol:         _Z15gemm_qkv_kernelPKDF16_S0_PDF16_S1_S1_PKfS3_S3_S3_S3_S1_PKiPyPj.kd
    .uniform_work_group_size: 1
    .uses_dynamic_stack: false
    .vgpr_count:     244
    .vgpr_spill_count: 0
    .wavefront_size: 64
  - .agpr_count:     0
    .args:
      - .address_space:  global
        .offset:         0
        .size:           8
        .value_kind:     global_buffer
      - .address_space:  global
        .offset:         8
        .size:           8
        .value_kind:     global_buffer
      - .address_space:  global
        .offset:         16
        .size:           8
        .value_kind:     global_buffer
    .group_segment_fixed_size: 0
    .kernarg_segment_align: 8
    .kernarg_segment_size: 24
    .language:       OpenCL C
    .language_version:
      - 2
      - 0
    .max_flat_workgroup_size: 512
    .name:           _Z15gemm_out_kernelPKDF16_S0_Pf
    .private_segment_fixed_size: 0
    .sgpr_count:     26
    .sgpr_spill_count: 0
    .symbol:         _Z15gemm_out_kernelPKDF16_S0_Pf.kd
    .uniform_work_group_size: 1
    .uses_dynamic_stack: false
    .vgpr_count:     148
    .vgpr_spill_count: 0
    .wavefront_size: 64
  - .agpr_count:     0
    .args:
      - .address_space:  global
        .offset:         0
        .size:           8
        .value_kind:     global_buffer
      - .address_space:  global
        .offset:         8
        .size:           8
        .value_kind:     global_buffer
      - .address_space:  global
        .offset:         16
        .size:           8
        .value_kind:     global_buffer
      - .address_space:  global
        .offset:         24
        .size:           8
        .value_kind:     global_buffer
      - .address_space:  global
        .offset:         32
        .size:           8
        .value_kind:     global_buffer
      - .address_space:  global
        .offset:         40
        .size:           8
        .value_kind:     global_buffer
    .group_segment_fixed_size: 0
    .kernarg_segment_align: 8
    .kernarg_segment_size: 48
    .language:       OpenCL C
    .language_version:
      - 2
      - 0
    .max_flat_workgroup_size: 512
    .name:           _Z11attn_kernelPKDF16_S0_S0_PDF16_PKjS3_
    .private_segment_fixed_size: 0
    .sgpr_count:     68
    .sgpr_spill_count: 0
    .symbol:         _Z11attn_kernelPKDF16_S0_S0_PDF16_PKjS3_.kd
    .uniform_work_group_size: 1
    .uses_dynamic_stack: false
    .vgpr_count:     248
    .vgpr_spill_count: 0
    .wavefront_size: 64
